# baseline (speedup 1.0000x reference)
.Lstag_loop_p3:
	s_sleep 0
	s_add_i32 s20, s20, -1
	s_cmp_lg_u32 s20, 0
	s_cbranch_scc1 .Lstag_loop_p3
